# retention output phase: three more head-of-body operand loads hoisted into free VGPRs (eleven in total issued with the first batch)
# baseline (speedup 1.0000x reference)
; __device__ __forceinline__ f32x4 mfma16(bf16x8 a, bf16x8 b, f32x4 c) { return __builtin_amdgcn_mfma_f32_16x16x32_bf16(a, b, c, 0, 0, 0); }
; __device__ __forceinline__ void ret_task(const Frame& F, int l, int task) {
;     ...
;     bf16x8 Qf[2][4], Kf[2][2][4];
; #pragma unroll
;     for (int qb = 0; qb < 2; ++qb)
; #pragma unroll
;         for (int ks = 0; ks < 4; ++ks) Qf[qb][ks] = ld_b8(TOK + (size_t)(tq0 + qb * 16 + c) * TOKP + TK_QR + h * HD + ks * 32 + rq * 8);
; #pragma unroll
;     for (int g = 0; g < 2; ++g)
; #pragma unroll
;         for (int ab = 0; ab < 2; ++ab) { const int key = 32 * g + (c >> 2) * 8 + 4 * ab + (c & 3);
; #pragma unroll
;             for (int ks = 0; ks < 4; ++ks) Kf[g][ab][ks] = ld_b8(TOK + (size_t)(tc0 + key) * TOKP + TK_KR + h * HD + rq * 8 + ks * 32); }
;     f32x4 acc[2][8];
; #pragma unroll
;     for (int qb = 0; qb < 2; ++qb)
; #pragma unroll
;         for (int eb = 0; eb < 8; ++eb) acc[qb][eb] = (f32x4){0.f, 0.f, 0.f, 0.f};
;     const bf16* sp = ST + (((size_t)bhh * NCH + n) * HD + c) * HD + rq * 8;
; #pragma unroll
;     for (int eb = 0; eb < 8; ++eb)
; #pragma unroll
;         for (int ks = 0; ks < 4; ++ks) { const bf16x8 sf = ld_b8(sp + eb * 16 * HD + ks * 32);
; #pragma unroll
;             for (int qb = 0; qb < 2; ++qb) acc[qb][eb] = mfma16(sf, Qf[qb][ks], acc[qb][eb]); }
.LBB0_655:
	s_bfe_u32 s1, s8, 0x50001
	s_ashr_i32 s0, s8, 9
	s_lshl_b32 s4, s0, 3
	s_lshl_b32 s0, s0, 11
	s_lshl_b32 s5, s1, 6
	v_and_b32_e32 v180, 15, v118
	s_or_b32 s0, s5, s0
	v_readlane_b32 s5, v251, 32
	v_ashrrev_i32_e32 v205, 4, v118
	s_or_b32 s4, s4, s9
	v_or_b32_e32 v209, s5, v180
	v_or_b32_e32 v196, s0, v209
	v_lshlrev_b32_e32 v202, 3, v205
	v_mov_b64_e32 v[160:161], s[80:81]
	s_movk_i32 s7, 0x2900
	s_ashr_i32 s5, s4, 31
	v_ashrrev_i32_e32 v203, 31, v202
	v_mad_i64_i32 v[198:199], s[12:13], v196, s7, v[160:161]
	s_lshl_b32 s96, s9, 8
	s_lshl_b64 s[4:5], s[4:5], 12
	s_lshl_b32 s1, s1, 7
	s_waitcnt lgkmcnt(0)
	v_lshl_add_u64 v[0:1], v[198:199], 0, s[96:97]
	v_lshlrev_b64 v[176:177], 1, v[202:203]
	s_or_b32 s1, s4, s1
	v_lshl_add_u64 v[8:9], v[0:1], 0, v[176:177]
	v_mov_b32_e32 v0, s1
	v_mov_b32_e32 v1, s5
	v_readlane_b32 s4, v253, 46
	v_lshlrev_b64 v[0:1], 8, v[0:1]
	v_readlane_b32 s5, v253, 47
	v_or_b32_e32 v194, 16, v196
	s_movk_i32 s6, 0x1000
	v_lshl_add_u64 v[0:1], s[4:5], 0, v[0:1]
	v_mad_i64_i32 v[200:201], s[4:5], v194, s7, v[160:161]
	v_add_co_u32_e32 v4, vcc, s6, v8
	s_mov_b64 s[4:5], 0x1000
	v_lshlrev_b32_e32 v2, 4, v180
	v_lshl_or_b32 v2, v205, 8, v2
	v_mov_b32_e32 v3, 0
	v_lshl_add_u64 v[36:37], v[0:1], 0, v[2:3]
	v_addc_co_u32_e32 v5, vcc, 0, v9, vcc
	v_lshl_add_u64 v[8:9], v[8:9], 0, s[4:5]
	global_load_dwordx4 v[0:3], v[36:37], off
	global_load_dwordx4 v[46:49], v[36:37], off offset:1024
	v_and_b32_e32 v242, -16, v196
	v_lshlrev_b32_e32 v242, 12, v242
	v_lshl_add_u32 v242, v180, 4, v242
	v_lshl_add_u32 v242, v205, 8, v242
	s_lshl_b32 s100, s9, 12
	v_add_u32_e32 v242, s100, v242
	v_add_u32_e32 v242, 0xe000000, v242
	v_mov_b32_e32 v243, 0
	v_mov_b32_e32 v238, s62
	v_mov_b32_e32 v239, s63
	v_lshl_add_u64 v[238:239], v[238:239], 0, v[242:243]
	v_mov_b32_e32 v242, 0x10000
	v_lshl_add_u64 v[240:241], v[238:239], 0, v[242:243]
	v_and_b32_e32 v242, -16, v196
	v_lshlrev_b32_e32 v242, 11, v242
	v_lshl_add_u32 v242, v180, 4, v242
	v_lshrrev_b32_e32 v243, 1, v205
	v_lshl_add_u32 v242, v243, 8, v242
	v_and_b32_e32 v243, 1, v205
	v_lshl_add_u32 v242, v243, 3, v242
	v_add_u32_e32 v242, s100, v242
	v_add_u32_e32 v242, 0x2ec00000, v242
	v_mov_b32_e32 v243, 0
	v_mov_b32_e32 v248, s62
	v_mov_b32_e32 v249, s63
	v_lshl_add_u64 v[248:249], v[248:249], 0, v[242:243]
	global_load_dwordx4 v[20:23], v[238:239], off
	global_load_dwordx4 v[52:55], v[238:239], off offset:1024
	v_lshl_add_u64 v[4:5], v[200:201], 0, s[96:97]
	v_lshl_add_u64 v[12:13], v[4:5], 0, v[176:177]
	v_add_co_u32_e32 v4, vcc, s6, v12
	v_lshl_add_u64 v[80:81], v[12:13], 0, s[4:5]
	s_nop 0
	v_addc_co_u32_e32 v5, vcc, 0, v13, vcc
	global_load_dwordx4 v[24:27], v[240:241], off
	global_load_dwordx4 v[60:63], v[238:239], off offset:2048
	global_load_dwordx4 v[56:59], v[240:241], off offset:1024
	global_load_dwordx4 v[64:67], v[240:241], off offset:2048
	s_movk_i32 s1, 0x2000
	v_add_co_u32_e32 v10, vcc, s1, v36
	s_movk_i32 s1, 0x4000
	s_nop 0
	v_addc_co_u32_e32 v11, vcc, 0, v37, vcc
	s_waitcnt lgkmcnt(0)
	global_load_dwordx4 v[14:17], v[10:11], off offset:-4096
	global_load_dwordx4 v[72:75], v[238:239], off offset:3072
	s_waitcnt vmcnt(19)
	v_add_co_u32_e32 v50, vcc, s1, v36
	global_load_dwordx4 v[28:31], v[10:11], off
	s_nop 0
	v_addc_co_u32_e32 v51, vcc, 0, v37, vcc
	v_add_co_u32_e32 v84, vcc, s6, v36
	global_load_dwordx4 v[38:41], v[50:51], off offset:-4096
	global_load_dwordx4 v[112:115], v[50:51], off offset:2048
	v_addc_co_u32_e32 v85, vcc, 0, v37, vcc
	global_load_dwordx4 v[120:123], v[84:85], off offset:1024
	global_load_dwordx4 v[124:127], v[10:11], off offset:1024
	global_load_dwordx4 v[128:131], v[36:37], off offset:2048
	global_load_dwordx4 v[132:135], v[84:85], off offset:2048
	global_load_dwordx4 v[136:139], v[36:37], off offset:3072
	global_load_dwordx4 v[140:143], v[10:11], off offset:2048
	global_load_dwordx4 v[144:147], v[10:11], off offset:3072
	global_load_dwordx4 v[148:151], v[84:85], off offset:3072
	global_load_dwordx4 v[152:155], v[50:51], off offset:1024
	global_load_dwordx4 v[156:159], v[50:51], off
	global_load_dwordx4 v[164:167], v[50:51], off offset:3072
	s_movk_i32 s1, 0x3000
	v_lshlrev_b32_e32 v119, 1, v118
	v_and_b32_e32 v118, 3, v118
	s_mov_b64 s[10:11], 0x1800
	s_lshl_b32 s9, s9, 7
	v_or_b32_e32 v228, 16, v209
	v_mov_b32_e32 v210, v202
	v_mov_b32_e32 v195, v202
	s_waitcnt vmcnt(21)
	v_mfma_f32_16x16x32_bf16 v[4:7], v[0:3], v[20:23], 0
	global_load_dwordx4 v[80:83], v[240:241], off offset:3072
	s_waitcnt vmcnt(20)
	v_mfma_f32_16x16x32_bf16 v[0:3], v[0:3], v[24:27], 0
	v_mfma_f32_16x16x32_bf16 v[4:7], v[46:49], v[52:55], v[4:7]
	s_waitcnt vmcnt(18)
	v_mfma_f32_16x16x32_bf16 v[0:3], v[46:49], v[56:59], v[0:3]
	s_waitcnt vmcnt(16)
	v_mfma_f32_16x16x32_bf16 v[32:35], v[14:17], v[20:23], 0
	v_mfma_f32_16x16x32_bf16 v[14:17], v[14:17], v[24:27], 0
	s_waitcnt vmcnt(13)
	v_mfma_f32_16x16x32_bf16 v[68:71], v[38:41], v[20:23], 0
	s_waitcnt vmcnt(0)
	v_mfma_f32_16x16x32_bf16 v[12:15], v[120:123], v[56:59], v[14:17]
	s_nop 3
	v_mfma_f32_16x16x32_bf16 v[42:45], v[28:31], v[20:23], 0
	v_mfma_f32_16x16x32_bf16 v[28:31], v[28:31], v[24:27], 0
	v_mfma_f32_16x16x32_bf16 v[32:35], v[120:123], v[52:55], v[32:35]
	s_waitcnt vmcnt(0)
	v_mfma_f32_16x16x32_bf16 v[42:45], v[124:127], v[52:55], v[42:45]
	v_mfma_f32_16x16x32_bf16 v[16:19], v[124:127], v[56:59], v[28:31]
	s_nop 2
	s_waitcnt vmcnt(0)
	v_mfma_f32_16x16x32_bf16 v[76:79], v[132:135], v[64:67], v[12:15]
	s_nop 2
	v_mfma_f32_16x16x32_bf16 v[4:7], v[128:131], v[60:63], v[4:7]
	v_mfma_f32_16x16x32_bf16 v[0:3], v[128:131], v[64:67], v[0:3]
	v_mfma_f32_16x16x32_bf16 v[46:49], v[132:135], v[60:63], v[32:35]
	s_nop 2
	s_waitcnt vmcnt(0)
; __device__ __forceinline__ f32x4 mfma16(bf16x8 a, bf16x8 b, f32x4 c) { return __builtin_amdgcn_mfma_f32_16x16x32_bf16(a, b, c, 0, 0, 0); }
; __device__ __forceinline__ void ret_task(const Frame& F, int l, int task) {
;     ...
;     const bf16* sp = ST + (((size_t)bhh * NCH + n) * HD + c) * HD + rq * 8;
; #pragma unroll
;     for (int eb = 0; eb < 8; ++eb)
; #pragma unroll
;         for (int ks = 0; ks < 4; ++ks) { const bf16x8 sf = ld_b8(sp + eb * 16 * HD + ks * 32);
; #pragma unroll
;             for (int qb = 0; qb < 2; ++qb) acc[qb][eb] = mfma16(sf, Qf[qb][ks], acc[qb][eb]); }
;     bf16x8 Vf[8];
; #pragma unroll
;     for (int eb = 0; eb < 8; ++eb) Vf[eb] = ld_b8(SWP + (size_t)(SW_VR + h * HD + eb * 16 + c) * SWPP + tc0 + 8 * rq);
	v_mfma_f32_16x16x32_bf16 v[28:31], v[136:139], v[80:83], v[0:3]
	s_nop 2
	s_waitcnt vmcnt(0)
	v_mfma_f32_16x16x32_bf16 v[42:45], v[140:143], v[60:63], v[42:45]
	v_mfma_f32_16x16x32_bf16 v[16:19], v[140:143], v[64:67], v[16:19]
	v_mfma_f32_16x16x32_bf16 v[32:35], v[136:139], v[72:75], v[4:7]
	s_nop 2
	v_add_co_u32_e32 v84, vcc, s1, v36
	s_movk_i32 s1, 0x6000
	s_nop 0
	v_addc_co_u32_e32 v85, vcc, 0, v37, vcc
	s_waitcnt vmcnt(0)
	v_mfma_f32_16x16x32_bf16 v[12:15], v[148:151], v[72:75], v[46:49]
	s_nop 2
	global_load_dwordx4 v[46:49], v[84:85], off offset:1024
	v_add_co_u32_e32 v116, vcc, s1, v36
	v_mfma_f32_16x16x32_bf16 v[8:11], v[148:151], v[80:83], v[76:79]
	s_nop 0
	v_addc_co_u32_e32 v117, vcc, 0, v37, vcc
	s_movk_i32 s1, 0x5000
	v_mfma_f32_16x16x32_bf16 v[4:7], v[144:147], v[72:75], v[42:45]
	global_load_dwordx4 v[76:79], v[84:85], off offset:3072
	global_load_dwordx4 v[92:95], v[116:117], off
	global_load_dwordx4 v[88:91], v[116:117], off offset:1024
	global_load_dwordx4 v[42:45], v[84:85], off offset:2048
	v_mfma_f32_16x16x32_bf16 v[0:3], v[144:147], v[80:83], v[16:19]
	global_load_dwordx4 v[108:111], v[116:117], off offset:-4096
	v_mfma_f32_16x16x32_bf16 v[16:19], v[38:41], v[24:27], 0
	s_waitcnt vmcnt(5)
	v_mfma_f32_16x16x32_bf16 v[38:41], v[46:49], v[52:55], v[68:71]
	s_nop 2
	v_mfma_f32_16x16x32_bf16 v[16:19], v[46:49], v[56:59], v[16:19]
	s_waitcnt vmcnt(1)
	v_mfma_f32_16x16x32_bf16 v[38:41], v[42:45], v[60:63], v[38:41]
	v_mfma_f32_16x16x32_bf16 v[42:45], v[42:45], v[64:67], v[16:19]
	v_mfma_f32_16x16x32_bf16 v[16:19], v[76:79], v[72:75], v[38:41]
	s_nop 5
	v_add_co_u32_e32 v38, vcc, s1, v36
	v_mfma_f32_16x16x32_bf16 v[40:43], v[76:79], v[80:83], v[42:45]
	s_nop 0
	v_addc_co_u32_e32 v39, vcc, 0, v37, vcc
	global_load_dwordx4 v[96:99], v[38:39], off offset:3072
	global_load_dwordx4 v[104:107], v[38:39], off offset:1024
	global_load_dwordx4 v[100:103], v[38:39], off offset:2048
	s_waitcnt vmcnt(3)
	v_mfma_f32_16x16x32_bf16 v[44:47], v[156:159], v[20:23], 0
	s_movk_i32 s1, 0x7000
	v_mfma_f32_16x16x32_bf16 v[76:79], v[156:159], v[24:27], 0
	v_mfma_f32_16x16x32_bf16 v[44:47], v[152:155], v[52:55], v[44:47]
	v_mfma_f32_16x16x32_bf16 v[68:71], v[152:155], v[56:59], v[76:79]
	s_nop 5
	global_load_dwordx4 v[76:79], v[116:117], off offset:2048
	global_load_dwordx4 v[84:87], v[116:117], off offset:3072
	v_add_co_u32_e32 v116, vcc, s1, v36
	v_mfma_f32_16x16x32_bf16 v[44:47], v[112:115], v[60:63], v[44:47]
	s_nop 0
	v_addc_co_u32_e32 v117, vcc, 0, v37, vcc
	global_load_dwordx4 v[36:39], v[116:117], off offset:1024
	v_mfma_f32_16x16x32_bf16 v[112:115], v[112:115], v[64:67], v[68:71]
	s_ashr_i32 s1, s0, 31
	s_nop 1
	global_load_dwordx4 v[68:71], v[116:117], off
	s_waitcnt vmcnt(4)
	v_mfma_f32_16x16x32_bf16 v[44:47], v[164:167], v[72:75], v[44:47]
	v_mfma_f32_16x16x32_bf16 v[48:51], v[164:167], v[80:83], v[112:115]
	s_nop 2
	v_and_b32_e32 v112, 24, v119
	v_mfma_f32_16x16x32_bf16 v[120:123], v[108:111], v[20:23], 0
	v_or3_b32 v162, v118, v112, s0
	v_and_b32_e32 v242, -16, v162
	v_lshlrev_b32_e32 v242, 12, v242
	v_and_b32_e32 v243, 15, v162
	v_lshl_add_u32 v242, v243, 4, v242
	v_lshl_add_u32 v242, v205, 8, v242
	s_lshl_b32 s100, s9, 5
	s_add_i32 s100, s100, 0x8000
	v_add_u32_e32 v242, s100, v242
	v_add_u32_e32 v242, 0xe000000, v242
	v_mov_b32_e32 v243, 0
	v_mov_b32_e32 v244, s62
	v_mov_b32_e32 v245, s63
	v_lshl_add_u64 v[244:245], v[244:245], 0, v[242:243]
	v_mov_b32_e32 v242, 0x20000
	v_lshl_add_u64 v[246:247], v[244:245], 0, v[242:243]
	v_mad_i64_i32 v[118:119], s[4:5], v162, s7, v[160:161]
	v_mfma_f32_16x16x32_bf16 v[124:127], v[108:111], v[24:27], 0
	global_load_dwordx4 v[112:115], v[116:117], off offset:2048
	v_lshl_add_u64 v[118:119], v[118:119], 0, s[96:97]
	v_lshl_add_u64 v[128:129], v[118:119], 0, v[176:177]
	v_mfma_f32_16x16x32_bf16 v[120:123], v[104:107], v[52:55], v[120:123]
	v_add_co_u32_e32 v108, vcc, s6, v128
	v_mfma_f32_16x16x32_bf16 v[104:107], v[104:107], v[56:59], v[124:127]
	s_nop 0
	v_addc_co_u32_e32 v109, vcc, 0, v129, vcc
	v_lshl_add_u64 v[128:129], v[128:129], 0, s[10:11]
	v_or_b32_e32 v124, 4, v162
	v_mad_i64_i32 v[124:125], s[4:5], v124, s7, v[160:161]
	v_lshl_add_u64 v[124:125], v[124:125], 0, s[96:97]
	global_load_dwordx4 v[108:111], v[244:245], off
	v_lshl_add_u64 v[130:131], v[124:125], 0, v[176:177]
	global_load_dwordx4 v[124:127], v[244:245], off offset:1024
	v_mfma_f32_16x16x32_bf16 v[120:123], v[100:103], v[60:63], v[120:123]
	global_load_dwordx4 v[116:119], v[116:117], off offset:3072
	v_mfma_f32_16x16x32_bf16 v[100:103], v[100:103], v[64:67], v[104:107]
	s_nop 2
	v_add_co_u32_e32 v104, vcc, s6, v130
	v_mfma_f32_16x16x32_bf16 v[144:147], v[96:99], v[72:75], v[120:123]
	s_nop 0
	v_addc_co_u32_e32 v105, vcc, 0, v131, vcc
	v_or_b32_e32 v106, s9, v180
	global_load_dwordx4 v[120:123], v[244:245], off offset:64
	v_mfma_f32_16x16x32_bf16 v[148:151], v[96:99], v[80:83], v[100:103]
	global_load_dwordx4 v[168:171], v[244:245], off offset:2048
	global_load_dwordx4 v[96:99], v[244:245], off offset:3072
	v_mul_u32_u24_e32 v106, 0x4080, v106
	v_lshlrev_b32_e32 v184, 1, v106
	v_mfma_f32_16x16x32_bf16 v[100:103], v[92:95], v[20:23], 0
	v_or_b32_e32 v104, 32, v162
	v_lshl_add_u64 v[106:107], s[64:65], 0, v[184:185]
	v_mad_i64_i32 v[104:105], s[4:5], v104, s7, v[160:161]
	v_mfma_f32_16x16x32_bf16 v[92:95], v[92:95], v[24:27], 0
	v_lshl_add_u64 v[106:107], s[0:1], 1, v[106:107]
	v_lshl_add_u64 v[178:179], v[106:107], 0, v[176:177]
	v_lshlrev_b32_e32 v242, 4, v180
	v_lshl_add_u32 v242, v205, 8, v242
	v_lshl_add_u32 v242, s9, 15, v242
	v_lshl_add_u32 v242, s0, 5, v242
	v_add_u32_e32 v242, 0x30c00000, v242
	v_mov_b32_e32 v243, 0
	v_mov_b32_e32 v238, s62
	v_mov_b32_e32 v239, s63
	v_lshl_add_u64 v[238:239], v[238:239], 0, v[242:243]
	v_mov_b32_e32 v178, v238
	v_mov_b32_e32 v179, v239
	s_mov_b32 s4, 0x380000
	v_mfma_f32_16x16x32_bf16 v[100:103], v[88:91], v[52:55], v[100:103]
	v_add_co_u32_e32 v106, vcc, s4, v178
	v_lshl_add_u64 v[128:129], v[130:131], 0, s[10:11]
	v_mfma_f32_16x16x32_bf16 v[88:91], v[88:91], v[56:59], v[92:95]
	v_addc_co_u32_e32 v107, vcc, 0, v179, vcc
	s_waitcnt vmcnt(10)
; __device__ __forceinline__ f32x4 mfma16(bf16x8 a, bf16x8 b, f32x4 c) { return __builtin_amdgcn_mfma_f32_16x16x32_bf16(a, b, c, 0, 0, 0); }
; __device__ __forceinline__ float fexp2(float x) { return __builtin_amdgcn_exp2f(x); }
; __device__ __forceinline__ void ret_task(const Frame& F, int l, int task) {
;     ...
;     bf16x8 Vf[8];
; #pragma unroll
;     for (int eb = 0; eb < 8; ++eb) Vf[eb] = ld_b8(SWP + (size_t)(SW_VR + h * HD + eb * 16 + c) * SWPP + tc0 + 8 * rq);
; #pragma unroll
;     for (int qb = 0; qb < 2; ++qb) { const float f = fexp2((float)(qb2 * 32 + qb * 16 + c + 1) * lg);
; #pragma unroll
;         for (int eb = 0; eb < 8; ++eb) acc[qb][eb] *= f; }
;     f32x4 g4[8]; u32x2 gwq[2][8];
; #pragma unroll
;     for (int g = 0; g < 2; ++g) {
;         if (g <= qb2) {
;             f32x4 sa[2][2];
; #pragma unroll
;             for (int qb = 0; qb < 2; ++qb)
; #pragma unroll
;                 for (int ab = 0; ab < 2; ++ab) sa[qb][ab] = (f32x4){0.f, 0.f, 0.f, 0.f};
; #pragma unroll
;             for (int ab = 0; ab < 2; ++ab)
; #pragma unroll
;                 for (int ks = 0; ks < 4; ++ks)
; #pragma unroll
;                     for (int qb = 0; qb < 2; ++qb) sa[qb][ab] = mfma16(Kf[g][ab][ks], Qf[qb][ks], sa[qb][ab]);
;             bf16x8 Pf[2];
; #pragma unroll
;             for (int qb = 0; qb < 2; ++qb) {
;                 const int i = qb2 * 32 + qb * 16 + c;
; #pragma unroll
;                 for (int ab = 0; ab < 2; ++ab)
; #pragma unroll
;                     for (int e = 0; e < 4; ++e) { const int diff = i - (32 * g + 8 * rq + 4 * ab + e);
;                         sa[qb][ab][e] = diff >= 0 ? sa[qb][ab][e] * fexp2((float)diff * lg) : 0.f; }
	v_mfma_f32_16x16x32_bf16 v[92:95], v[76:79], v[60:63], v[100:103]
	v_mfma_f32_16x16x32_bf16 v[100:103], v[76:79], v[64:67], v[88:91]
	global_load_dwordx4 v[76:79], v[106:107], off
	global_load_dwordx4 v[172:175], v[244:245], off offset:1088
	s_nop 1
	v_lshl_add_u64 v[88:89], v[104:105], 0, s[96:97]
	s_waitcnt vmcnt(11)
	v_mfma_f32_16x16x32_bf16 v[152:155], v[84:87], v[72:75], v[92:95]
	v_lshl_add_u64 v[104:105], v[88:89], 0, v[176:177]
	global_load_dwordx4 v[88:91], v[244:245], off offset:3136
	v_lshl_add_u64 v[106:107], v[104:105], 0, s[10:11]
	v_mfma_f32_16x16x32_bf16 v[156:159], v[84:87], v[80:83], v[100:103]
	global_load_dwordx4 v[84:87], v[244:245], off offset:2112
	v_add_co_u32_e32 v104, vcc, s6, v104
	s_waitcnt vmcnt(11)
	v_mfma_f32_16x16x32_bf16 v[92:95], v[68:71], v[20:23], 0
	v_addc_co_u32_e32 v105, vcc, 0, v105, vcc
	global_load_dwordx4 v[132:135], v[246:247], off offset:1024
	global_load_dwordx4 v[128:131], v[246:247], off offset:2048
	v_mfma_f32_16x16x32_bf16 v[100:103], v[68:71], v[24:27], 0
	v_or_b32_e32 v68, 36, v162
	v_mad_i64_i32 v[68:69], s[4:5], v68, s7, v[160:161]
	v_mfma_f32_16x16x32_bf16 v[92:95], v[36:39], v[52:55], v[92:95]
	s_mov_b32 s4, 0
	v_add_co_u32_e32 v70, vcc, s4, v178
	v_mfma_f32_16x16x32_bf16 v[36:39], v[36:39], v[56:59], v[100:103]
	s_nop 0
	v_addc_co_u32_e32 v71, vcc, 0, v179, vcc
	s_mov_b32 s4, 0x80000
	s_waitcnt vmcnt(12)
	v_mfma_f32_16x16x32_bf16 v[36:39], v[112:115], v[64:67], v[36:39]
	global_load_dwordx4 v[140:143], v[246:247], off
	global_load_dwordx4 v[136:139], v[246:247], off offset:3072
	v_lshl_add_u64 v[68:69], v[68:69], 0, s[96:97]
	v_lshl_add_u64 v[68:69], v[68:69], 0, v[176:177]
	v_mfma_f32_16x16x32_bf16 v[100:103], v[112:115], v[60:63], v[92:95]
	s_nop 2
	global_load_dwordx4 v[92:95], v[70:71], off
	v_add_co_u32_e32 v70, vcc, s4, v178
	s_mov_b32 s4, 0x100000
	s_nop 0
	v_addc_co_u32_e32 v71, vcc, 0, v179, vcc
	v_add_co_u32_e32 v104, vcc, s4, v178
	s_waitcnt vmcnt(12)
	v_mfma_f32_16x16x32_bf16 v[164:167], v[116:119], v[80:83], v[36:39]
	v_addc_co_u32_e32 v105, vcc, 0, v179, vcc
	s_mov_b32 s4, 0x180000
	v_mfma_f32_16x16x32_bf16 v[36:39], v[108:111], v[20:23], 0
	v_mfma_f32_16x16x32_bf16 v[108:111], v[108:111], v[24:27], 0
	v_mfma_f32_16x16x32_bf16 v[160:163], v[116:119], v[72:75], v[100:103]
	s_nop 2
	global_load_dwordx4 v[100:103], v[70:71], off
	s_nop 0
	global_load_dwordx4 v[104:107], v[104:105], off
	v_add_co_u32_e32 v70, vcc, s4, v178
	s_mov_b32 s4, 0x200000
	s_nop 0
	v_addc_co_u32_e32 v71, vcc, 0, v179, vcc
	v_add_co_u32_e32 v116, vcc, s4, v178
	v_readlane_b32 s4, v251, 33
	s_nop 0
	v_addc_co_u32_e32 v117, vcc, 0, v179, vcc
	v_mfma_f32_16x16x32_bf16 v[36:39], v[124:127], v[52:55], v[36:39]
	global_load_dwordx4 v[112:115], v[70:71], off
	s_nop 0
	global_load_dwordx4 v[116:119], v[116:117], off
	v_add_u32_e32 v70, s4, v180
	v_cvt_f32_ubyte0_e32 v71, v70
	v_mfma_f32_16x16x32_bf16 v[108:111], v[124:127], v[56:59], v[108:111]
	v_add_u32_e32 v70, 16, v70
	v_cvt_f32_ubyte0_e32 v70, v70
	v_or_b32_e32 v126, 2, v202
	v_mul_f32_e32 v71, v197, v71
	v_mul_f32_e32 v70, v197, v70
	s_waitcnt vmcnt(14)
	v_mfma_f32_16x16x32_bf16 v[36:39], v[168:171], v[60:63], v[36:39]
	v_exp_f32_e32 v204, v71
	v_exp_f32_e32 v206, v70
	v_or_b32_e32 v127, 3, v202
	v_mfma_f32_16x16x32_bf16 v[108:111], v[168:171], v[64:67], v[108:111]
	v_sub_u32_e32 v169, v209, v202
	v_sub_u32_e32 v170, v209, v126
	v_cvt_f32_u32_e32 v70, v169
	v_cvt_f32_u32_e32 v71, v170
	s_waitcnt vmcnt(13)
	v_mfma_f32_16x16x32_bf16 v[36:39], v[96:99], v[72:75], v[36:39]
	v_or_b32_e32 v168, 1, v202
	v_mul_f32_e32 v70, v197, v70
	v_mul_f32_e32 v71, v197, v71
	v_exp_f32_e32 v70, v70
	v_exp_f32_e32 v71, v71
	v_mfma_f32_16x16x32_bf16 v[96:99], v[96:99], v[80:83], v[108:111]
	s_nop 1
	v_mov_b32_e32 v124, v36
	v_mov_b32_e32 v125, v38
	v_pk_mul_f32 v[70:71], v[70:71], v[124:125]
	v_mfma_f32_16x16x32_bf16 v[108:111], v[120:123], v[20:23], 0
	v_cmp_lt_i32_e32 vcc, -1, v170
	v_sub_u32_e32 v125, v209, v127
	v_cvt_f32_u32_e32 v38, v125
	v_mfma_f32_16x16x32_bf16 v[120:123], v[120:123], v[24:27], 0
	v_cndmask_b32_e32 v124, 0, v71, vcc
	v_sub_u32_e32 v71, v209, v168
	v_cvt_f32_u32_e32 v36, v71
	s_waitcnt vmcnt(11)
	v_mfma_f32_16x16x32_bf16 v[108:111], v[172:175], v[52:55], v[108:111]
	v_cmp_lt_i32_e32 vcc, -1, v169
	v_pk_mul_f32 v[14:15], v[204:205], v[14:15] op_sel_hi:[0,1]
	v_mul_f32_e32 v36, v197, v36
	v_mfma_f32_16x16x32_bf16 v[120:123], v[172:175], v[56:59], v[120:123]
	v_mul_f32_e64 v12, v204, v12
	v_mul_f32_e64 v13, v204, v13
	s_mov_b32 s4, 0x280000
	v_pk_mul_f32 v[6:7], v[204:205], v[6:7] op_sel_hi:[0,1]
	s_waitcnt vmcnt(9)
; __device__ __forceinline__ f32x4 mfma16(bf16x8 a, bf16x8 b, f32x4 c) { return __builtin_amdgcn_mfma_f32_16x16x32_bf16(a, b, c, 0, 0, 0); }
; __device__ __forceinline__ float fexp2(float x) { return __builtin_amdgcn_exp2f(x); }
; __device__ __forceinline__ void ret_task(const Frame& F, int l, int task) {
;     ...
;             bf16x8 Pf[2];
; #pragma unroll
;             for (int qb = 0; qb < 2; ++qb) {
;                 const int i = qb2 * 32 + qb * 16 + c;
; #pragma unroll
;                 for (int ab = 0; ab < 2; ++ab)
; #pragma unroll
;                     for (int e = 0; e < 4; ++e) { const int diff = i - (32 * g + 8 * rq + 4 * ab + e);
;                         sa[qb][ab][e] = diff >= 0 ? sa[qb][ab][e] * fexp2((float)diff * lg) : 0.f; }
;                 Pf[qb] = pack8(sa[qb][0], sa[qb][1]);
;             }
; #pragma unroll
;             for (int eb = 0; eb < 8; ++eb)
; #pragma unroll
;                 for (int qb = 0; qb < 2; ++qb) acc[qb][eb] = mfma16(Vf[eb], Pf[qb], acc[qb][eb]);
	v_mfma_f32_16x16x32_bf16 v[108:111], v[84:87], v[60:63], v[108:111]
	v_mul_f32_e64 v4, v204, v4
	v_mul_f32_e64 v5, v204, v5
	v_pk_mul_f32 v[30:31], v[206:207], v[30:31] op_sel_hi:[0,1]
	v_pk_mul_f32 v[28:29], v[206:207], v[28:29] op_sel_hi:[0,1]
	v_mfma_f32_16x16x32_bf16 v[84:87], v[84:87], v[64:67], v[120:123]
	v_mul_f32_e64 v2, v206, v2
	v_mul_f32_e64 v3, v206, v3
	v_pk_mul_f32 v[0:1], v[206:207], v[0:1] op_sel_hi:[0,1]
	v_pk_mul_f32 v[34:35], v[204:205], v[34:35] op_sel_hi:[0,1]
	v_exp_f32_e32 v120, v36
	v_mul_f32_e32 v36, v197, v38
	v_exp_f32_e32 v121, v36
	v_mov_b32_e32 v38, v37
	v_cndmask_b32_e32 v122, 0, v70, vcc
	v_cmp_lt_i32_e32 vcc, -1, v71
	v_pk_mul_f32 v[36:37], v[120:121], v[38:39]
	v_mfma_f32_16x16x32_bf16 v[108:111], v[88:91], v[72:75], v[108:111]
	v_sub_u32_e32 v39, v228, v126
	v_cvt_f32_u32_e32 v70, v39
	v_sub_u32_e32 v120, v228, v127
	v_mfma_f32_16x16x32_bf16 v[84:87], v[88:91], v[80:83], v[84:87]
	v_cndmask_b32_e32 v88, 0, v36, vcc
	v_cmp_lt_i32_e32 vcc, -1, v125
	v_sub_u32_e32 v91, v228, v168
	v_sub_u32_e32 v89, v228, v202
	v_cndmask_b32_e32 v90, 0, v37, vcc
	v_cvt_f32_u32_e32 v37, v91
	v_cvt_f32_u32_e32 v36, v89
	v_mov_b32_e32 v71, v98
	v_cmp_lt_i32_e32 vcc, -1, v39
	v_mul_f32_e32 v37, v197, v37
	v_mul_f32_e32 v36, v197, v36
	v_exp_f32_e32 v38, v37
	v_mul_f32_e32 v37, v197, v70
	v_exp_f32_e32 v36, v36
	v_exp_f32_e32 v37, v37
	v_mov_b32_e32 v70, v96
	v_cvt_f32_u32_e32 v96, v120
	v_mov_b32_e32 v98, v97
	v_pk_mul_f32 v[36:37], v[36:37], v[70:71]
	v_or_b32_e32 v123, 5, v202
	v_cndmask_b32_e32 v121, 0, v37, vcc
	v_mul_f32_e32 v37, v197, v96
	v_exp_f32_e32 v39, v37
	v_cmp_lt_i32_e32 vcc, -1, v89
	v_or_b32_e32 v97, 6, v202
	v_sub_u32_e32 v125, v209, v123
	v_cndmask_b32_e32 v89, 0, v36, vcc
	v_pk_mul_f32 v[36:37], v[38:39], v[98:99]
	v_cmp_lt_i32_e32 vcc, -1, v91
	v_or_b32_e32 v98, 4, v202
	v_sub_u32_e32 v99, v209, v98
	v_cndmask_b32_e32 v91, 0, v36, vcc
	v_cmp_lt_i32_e32 vcc, -1, v120
	v_sub_u32_e32 v39, v209, v97
	v_cvt_f32_u32_e32 v36, v99
	v_cndmask_b32_e32 v96, 0, v37, vcc
	v_cvt_f32_u32_e32 v37, v125
	v_cvt_f32_u32_e32 v70, v39
	v_or_b32_e32 v120, 7, v202
	v_mul_f32_e32 v36, v197, v36
	v_mul_f32_e32 v37, v197, v37
	v_exp_f32_e32 v38, v37
	v_mul_f32_e32 v37, v197, v70
	v_exp_f32_e32 v36, v36
	v_sub_u32_e32 v126, v209, v120
	v_exp_f32_e32 v37, v37
	v_mov_b32_e32 v70, v108
	v_cvt_f32_u32_e32 v108, v126
	v_mov_b32_e32 v71, v110
	v_pk_mul_f32 v[36:37], v[36:37], v[70:71]
	v_cmp_lt_i32_e32 vcc, -1, v39
	v_mov_b32_e32 v110, v109
	v_sub_u32_e32 v98, v228, v98
	v_cndmask_b32_e32 v127, 0, v37, vcc
	v_mul_f32_e32 v37, v197, v108
	v_exp_f32_e32 v39, v37
	v_cmp_lt_i32_e32 vcc, -1, v99
	v_mov_b32_e32 v71, v86
	v_mov_b32_e32 v86, v85
	v_cndmask_b32_e32 v99, 0, v36, vcc
	v_pk_mul_f32 v[36:37], v[38:39], v[110:111]
	v_cmp_lt_i32_e32 vcc, -1, v125
	v_sub_u32_e32 v39, v228, v97
	v_sub_u32_e32 v97, v228, v123
	v_cndmask_b32_e32 v108, 0, v36, vcc
	v_cmp_lt_i32_e32 vcc, -1, v126
	v_cvt_f32_u32_e32 v36, v98
	v_cvt_f32_u32_e32 v70, v39
	v_cndmask_b32_e32 v109, 0, v37, vcc
	v_cvt_f32_u32_e32 v37, v97
	v_mul_f32_e32 v36, v197, v36
	v_exp_f32_e32 v36, v36
	v_sub_u32_e32 v110, v228, v120
	v_mul_f32_e32 v37, v197, v37
	v_exp_f32_e32 v38, v37
	v_mul_f32_e32 v37, v197, v70
	v_exp_f32_e32 v37, v37
	v_mov_b32_e32 v70, v84
	v_cvt_f32_u32_e32 v84, v110
	v_cmp_lt_i32_e32 vcc, -1, v39
	v_pk_mul_f32 v[36:37], v[36:37], v[70:71]
	s_nop 0
	v_cndmask_b32_e32 v70, 0, v37, vcc
	v_mul_f32_e32 v37, v197, v84
	v_exp_f32_e32 v39, v37
	v_cmp_lt_i32_e32 vcc, -1, v98
	s_nop 1
	v_cndmask_b32_e32 v71, 0, v36, vcc
	v_pk_mul_f32 v[36:37], v[38:39], v[86:87]
	v_bfe_u32 v38, v90, 16, 1
	v_bfe_u32 v39, v88, 16, 1
	v_add3_u32 v39, v88, v39, s76
	v_add3_u32 v38, v90, v38, s76
	s_nop 1
	v_bfe_u32 v88, v122, 16, 1
	v_bfe_u32 v90, v124, 16, 1
	v_cmp_lt_i32_e32 vcc, -1, v97
	v_add3_u32 v90, v124, v90, s76
	v_add3_u32 v88, v122, v88, s76
	s_nop 1
	v_cndmask_b32_e32 v36, 0, v36, vcc
	v_cmp_lt_i32_e32 vcc, -1, v110
	s_nop 2
	v_lshrrev_b32_e32 v88, 16, v88
	v_lshrrev_b32_e32 v90, 16, v90
	v_cndmask_b32_e32 v37, 0, v37, vcc
	v_and_or_b32 v231, v38, s75, v90
	v_and_or_b32 v230, v39, s75, v88
	v_cvt_pk_bf16_f32 v233, v127, v109
	v_cvt_pk_bf16_f32 v232, v99, v108
	v_bfe_u32 v84, v96, 16, 1
	v_bfe_u32 v38, v37, 16, 1
	v_add3_u32 v84, v96, v84, s76
	s_waitcnt vmcnt(3)
	v_mfma_f32_16x16x32_bf16 v[96:99], v[100:103], v[230:233], v[12:15]
	v_bfe_u32 v39, v36, 16, 1
	v_bfe_u32 v85, v91, 16, 1
	v_add3_u32 v37, v37, v38, s76
	v_add_co_u32_e32 v12, vcc, s4, v178
	v_bfe_u32 v38, v89, 16, 1
	s_nop 0
	v_addc_co_u32_e32 v13, vcc, 0, v179, vcc
	s_mov_b32 s4, 0x300000
	v_add3_u32 v85, v91, v85, s76
	v_add3_u32 v36, v36, v39, s76
	v_bfe_u32 v39, v121, 16, 1
	v_add3_u32 v38, v89, v38, s76
	s_waitcnt vmcnt(2)
; __device__ __forceinline__ f32x4 mfma16(bf16x8 a, bf16x8 b, f32x4 c) { return __builtin_amdgcn_mfma_f32_16x16x32_bf16(a, b, c, 0, 0, 0); }
; __device__ __forceinline__ void ret_task(const Frame& F, int l, int task) {
;     ...
; #pragma unroll
;             for (int eb = 0; eb < 8; ++eb)
; #pragma unroll
;                 for (int qb = 0; qb < 2; ++qb) acc[qb][eb] = mfma16(Vf[eb], Pf[qb], acc[qb][eb]);
;         }
;         if (g == 0) {
;             if (qb2) {
; #pragma unroll
;                 for (int eb = 0; eb < 8; ++eb) Vf[eb] = ld_b8(SWP + (size_t)(SW_VR + h * HD + eb * 16 + c) * SWPP + tc0 + 32 + 8 * rq);
;             }
	v_mfma_f32_16x16x32_bf16 v[88:91], v[104:107], v[230:233], v[4:7]
	v_add3_u32 v39, v121, v39, s76
	global_load_dwordx4 v[120:123], v[12:13], off
	v_bfe_u32 v86, v71, 16, 1
	v_add_co_u32_e32 v4, vcc, s4, v178
	v_bfe_u32 v87, v70, 16, 1
	s_nop 0
	v_addc_co_u32_e32 v5, vcc, 0, v179, vcc
	global_load_dwordx4 v[124:127], v[4:5], off
	v_add_co_u32_e32 v6, vcc, s6, v68
	v_lshl_add_u64 v[4:5], v[68:69], 0, s[10:11]
	s_nop 0
	v_addc_co_u32_e32 v7, vcc, 0, v69, vcc
	global_load_dwordx4 v[172:175], v[246:247], off offset:1088
	global_load_dwordx4 v[168:171], v[246:247], off offset:2112
	global_load_dwordx4 v[180:183], v[246:247], off offset:64
	global_load_dwordx4 v[176:179], v[246:247], off offset:3136
	v_add3_u32 v70, v70, v87, s76
	v_add3_u32 v71, v71, v86, s76
	v_lshrrev_b32_e32 v38, 16, v38
	v_lshrrev_b32_e32 v39, 16, v39
	v_lshrrev_b32_e32 v71, 16, v71
	v_lshrrev_b32_e32 v70, 16, v70
	v_and_or_b32 v237, v37, s75, v70
	v_and_or_b32 v236, v36, s75, v71
	v_and_or_b32 v235, v84, s75, v39
	v_and_or_b32 v234, v85, s75, v38
	v_readlane_b32 s4, v251, 34
	v_pk_mul_f32 v[32:33], v[204:205], v[32:33] op_sel_hi:[0,1]
	v_mfma_f32_16x16x32_bf16 v[36:39], v[92:95], v[234:237], v[28:31]
	v_mul_f32_e64 v10, v206, v10
	v_mul_f32_e64 v11, v206, v11
	v_pk_mul_f32 v[8:9], v[206:207], v[8:9] op_sel_hi:[0,1]
	v_pk_mul_f32 v[6:7], v[206:207], v[150:151] op_sel_hi:[0,1]
	v_mfma_f32_16x16x32_bf16 v[28:31], v[104:107], v[234:237], v[0:3]
	v_mul_f32_e64 v4, v206, v148
	v_mul_f32_e64 v5, v206, v149
	v_readlane_b32 s5, v251, 35
	s_andn2_b64 vcc, exec, s[4:5]
	v_pk_mul_f32 v[2:3], v[204:205], v[18:19] op_sel_hi:[0,1]
	v_pk_mul_f32 v[0:1], v[204:205], v[16:17] op_sel_hi:[0,1]
	v_mfma_f32_16x16x32_bf16 v[108:111], v[92:95], v[230:233], v[32:35]
	s_waitcnt vmcnt(7)
	v_mfma_f32_16x16x32_bf16 v[84:87], v[112:115], v[230:233], v[0:3]
	s_nop 2
	v_mul_f32_e64 v2, v206, v42
	v_mul_f32_e64 v3, v206, v43
	v_pk_mul_f32 v[0:1], v[206:207], v[40:41] op_sel_hi:[0,1]
	v_mfma_f32_16x16x32_bf16 v[32:35], v[100:103], v[234:237], v[8:11]
	v_mul_f32_e64 v42, v204, v162
	v_mul_f32_e64 v43, v204, v163
	v_pk_mul_f32 v[40:41], v[204:205], v[160:161] op_sel_hi:[0,1]
	v_mfma_f32_16x16x32_bf16 v[16:19], v[112:115], v[234:237], v[0:3]
	s_nop 2
	v_mul_f32_e64 v2, v204, v46
	v_mul_f32_e64 v3, v204, v47
	v_pk_mul_f32 v[0:1], v[204:205], v[44:45] op_sel_hi:[0,1]
	s_waitcnt vmcnt(5)
	v_mfma_f32_16x16x32_bf16 v[8:11], v[120:123], v[234:237], v[4:7]
	v_mfma_f32_16x16x32_bf16 v[68:71], v[116:119], v[230:233], v[0:3]
	s_nop 2
	v_mul_f32_e64 v2, v206, v50
	v_mul_f32_e64 v3, v206, v51
	v_pk_mul_f32 v[0:1], v[206:207], v[48:49] op_sel_hi:[0,1]
	v_mfma_f32_16x16x32_bf16 v[40:43], v[76:79], v[230:233], v[40:43]
	s_nop 0
	v_mfma_f32_16x16x32_bf16 v[12:15], v[116:119], v[234:237], v[0:3]
	s_nop 2
	v_mul_f32_e64 v2, v204, v146
	v_mul_f32_e64 v3, v204, v147
	v_pk_mul_f32 v[0:1], v[204:205], v[144:145] op_sel_hi:[0,1]
	v_pk_mul_f32 v[146:147], v[206:207], v[166:167] op_sel_hi:[0,1]
	v_pk_mul_f32 v[144:145], v[206:207], v[164:165] op_sel_hi:[0,1]
	v_mfma_f32_16x16x32_bf16 v[48:51], v[120:123], v[230:233], v[0:3]
	s_nop 2
	v_mul_f32_e64 v2, v204, v154
	v_mul_f32_e64 v3, v204, v155
	v_pk_mul_f32 v[0:1], v[204:205], v[152:153] op_sel_hi:[0,1]
	s_waitcnt vmcnt(4)
	s_nop 0
	v_mfma_f32_16x16x32_bf16 v[44:47], v[124:127], v[230:233], v[0:3]
	s_nop 2
	v_mul_f32_e64 v2, v206, v158
	v_mul_f32_e64 v3, v206, v159
	v_pk_mul_f32 v[0:1], v[206:207], v[156:157] op_sel_hi:[0,1]
	s_nop 1
	v_mfma_f32_16x16x32_bf16 v[4:7], v[124:127], v[234:237], v[0:3]
	s_nop 2
	v_cndmask_b32_e64 v0, 0, 1, s[4:5]
	v_cmp_ne_u32_e64 s[34:35], 1, v0
	v_mfma_f32_16x16x32_bf16 v[0:3], v[76:79], v[234:237], v[144:147]
	s_cbranch_vccnz .LBB0_657
	s_lshl_b64 s[0:1], s[0:1], 1
	s_add_u32 s0, s64, s0
	s_addc_u32 s1, s65, s1
	v_lshl_add_u64 v[76:77], s[0:1], 0, v[184:185]
	v_lshl_add_u64 v[76:77], v[202:203], 1, v[76:77]
	v_mov_b32_e32 v76, v238
	v_mov_b32_e32 v77, v239
	v_add_co_u32_e32 v78, vcc, 0, v76
	s_nop 1
	v_addc_co_u32_e32 v79, vcc, 0, v77, vcc
	v_add_co_u32_e32 v100, vcc, 0x80000, v76
	s_nop 1
	v_addc_co_u32_e32 v101, vcc, 0, v77, vcc
	global_load_dwordx4 v[92:95], v[78:79], off offset:1024
	s_nop 0
	global_load_dwordx4 v[100:103], v[100:101], off offset:1024
	v_add_co_u32_e32 v78, vcc, 0x100000, v76
	s_nop 1
	v_addc_co_u32_e32 v79, vcc, 0, v77, vcc
	v_add_co_u32_e32 v112, vcc, 0x180000, v76
	s_nop 1
	v_addc_co_u32_e32 v113, vcc, 0, v77, vcc
	global_load_dwordx4 v[104:107], v[78:79], off offset:1024
	s_nop 0
	global_load_dwordx4 v[112:115], v[112:113], off offset:1024
	v_add_co_u32_e32 v78, vcc, 0x200000, v76
	s_nop 1
	v_addc_co_u32_e32 v79, vcc, 0, v77, vcc
	v_add_co_u32_e32 v120, vcc, 0x280000, v76
	s_nop 1
	v_addc_co_u32_e32 v121, vcc, 0, v77, vcc
	global_load_dwordx4 v[116:119], v[78:79], off offset:1024
	s_nop 0
	global_load_dwordx4 v[120:123], v[120:121], off offset:1024
	v_add_co_u32_e32 v78, vcc, 0x300000, v76
	s_nop 1
	v_addc_co_u32_e32 v79, vcc, 0, v77, vcc
	v_add_co_u32_e32 v76, vcc, 0x380000, v76
	s_nop 1
	v_addc_co_u32_e32 v77, vcc, 0, v77, vcc
	global_load_dwordx4 v[124:127], v[78:79], off offset:1024
	s_nop 0
	global_load_dwordx4 v[76:79], v[76:77], off offset:1024
